# attention: row-max tree of the next tile computed under the current step's P.V MFMAs instead of after the step barrier (on v11)
# speedup vs baseline: 1.0067x; 1.0067x over previous
; __device__ __forceinline__ int opaque_tid() { int t = threadIdx.x; asm volatile("" : "+v"(t)); return t; }
; #define ATT_DMAK(tile, slot) do { _Pragma("unroll") for (int i = 0; i < 4; ++i) { const int pc = (wv + 8 * i) < 25 ? (wv + 8 * i) : 24; \
;         __builtin_amdgcn_global_load_lds((const unsigned*)((const char*)Kbh + (size_t)(tile) * (64 * 384) + doffK[i]), (LAS unsigned*)(lds + (slot) * KT_BYTES + pc * 1024), 16, 0, 0); } } while (0)
; #define ATT_DMAV(tile, slot) do { _Pragma("unroll") for (int i = 0; i < 3; ++i) { const int pc = (wv + 8 * i) < 18 ? (wv + 8 * i) : 17; \
;         __builtin_amdgcn_global_load_lds((const unsigned*)((const char*)Vbh + (size_t)(tile) * 128 + doffV[i]), (LAS unsigned*)(lds + VRING + (slot) * VT_BYTES + pc * 1024), 16, 0, 0); } } while (0)
; __device__ __forceinline__ void attn_unit(const bf16_t* Qrows  , const bf16_t* Kbh, const bf16_t* Vbh, int nkeys, bf16_t* Orows, LAS unsigned char* lds) {
;     const int tid = opaque_tid(), lane = tid & 63, wave = tid >> 6, l32 = lane & 31, hi = lane >> 5, qg = wave & 3, kh = wave >> 2;
;     constexpr int VRING = 3 * KT_BYTES;
;     bf16x8 qf[12];
;     { const bf16_t* qr = Qrows + (size_t)(qg * 32 + l32) * 768 + hi * 8;
; #pragma unroll
;       for (int ks = 0; ks < 12; ++ks) qf[ks] = *(const bf16x8*)(qr + ks * 16); }
;     f32x16 o[4];
; #pragma unroll
;     for (int db = 0; db < 4; ++db)
; #pragma unroll
;         for (int r = 0; r < 16; ++r) o[db][r] = 0.f;
;     float mrow = -1e30f, lsum = 0.f;
;     const int nt = nkeys / 64;
;     const int wv = __builtin_amdgcn_readfirstlane(wave);
;     unsigned doffK[4], doffV[3];
; #pragma unroll
;     for (int i = 0; i < 4; ++i) { const int pc = (wv + 8 * i) < 25 ? (wv + 8 * i) : 24; const int X = pc * 1024 + lane * 16, row = X / KPITCH, col = X % KPITCH; doffK[i] = (unsigned)(row * 384 + (col < 384 ? col : 0)); }
; #pragma unroll
;     for (int i = 0; i < 3; ++i) { const int pc = (wv + 8 * i) < 18 ? (wv + 8 * i) : 17; const int Y = pc * 1024 + lane * 16, row = Y / VPITCH, col = Y % VPITCH; doffV[i] = (unsigned)(row * (NKEY * 2) + (col < 128 ? col : 0)); }
;     ...
;     ATT_DMAK(0, 0); ATT_DMAV(0, 0); ATT_DMAK(1, 1); ATT_DMAV(1, 1); if (nt > 2) ATT_DMAK(2, 2);
;     asm volatile("s_waitcnt vmcnt(0)" ::: "memory");
;     __builtin_amdgcn_s_barrier(); asm volatile("" ::: "memory");
.LBB0_1234:
	s_lshl_b32 s1, s61, s1
	s_and_b32 s0, s1, s0
	s_or_b32 s54, s14, s0
	s_and_b32 s62, s13, 3
	s_ashr_i32 s55, s54, 31
	s_mul_i32 s1, s54, 0x600
	s_mul_hi_i32 s0, s54, 0x600
	s_add_u32 s1, s31, s1
	s_addc_u32 s0, s56, s0
	s_mul_i32 s13, s62, 0x180
	s_add_u32 s16, s1, s13
	s_addc_u32 s17, s0, 0
	s_lshl_b32 s0, s12, 2
	v_mov_b32_e32 v176, v0
	s_or_b32 s14, s62, s0
	s_mul_i32 s15, s14, 0xd8000
	v_ashrrev_i32_e32 v4, 6, v176
	v_and_b32_e32 v24, 31, v176
	v_and_b32_e32 v178, 3, v4
	s_mul_hi_i32 s13, s14, 0xd8000
	s_add_u32 s0, s57, s15
	v_lshl_or_b32 v175, v178, 5, v24
	v_mov_b64_e32 v[2:3], s[16:17]
	s_movk_i32 s16, 0x600
	s_addc_u32 s1, s58, s13
	s_mul_hi_i32 s12, s14, 0x90000
	s_mul_i32 s14, s14, 0x90000
	v_bfe_u32 v174, v176, 5, 1
	v_mad_u64_u32 v[2:3], s[16:17], v175, s16, v[2:3]
	s_add_u32 s24, s59, s14
	v_lshlrev_b32_e32 v206, 4, v174
	v_readfirstlane_b32 s16, v4
	s_addc_u32 s25, s60, s12
	v_and_b32_e32 v177, 63, v176
	v_lshl_add_u64 v[2:3], v[2:3], 0, v[206:207]
	s_min_i32 s17, s16, 24
	global_load_dwordx4 v[142:145], v[2:3], off
	global_load_dwordx4 v[138:141], v[2:3], off offset:32
	global_load_dwordx4 v[134:137], v[2:3], off offset:64
	global_load_dwordx4 v[130:133], v[2:3], off offset:96
	global_load_dwordx4 v[126:129], v[2:3], off offset:128
	global_load_dwordx4 v[122:125], v[2:3], off offset:160
	global_load_dwordx4 v[118:121], v[2:3], off offset:192
	global_load_dwordx4 v[114:117], v[2:3], off offset:224
	global_load_dwordx4 v[110:113], v[2:3], off offset:256
	global_load_dwordx4 v[106:109], v[2:3], off offset:288
	global_load_dwordx4 v[102:105], v[2:3], off offset:320
	global_load_dwordx4 v[98:101], v[2:3], off offset:352
	v_lshlrev_b32_e32 v3, 4, v177
	s_lshl_b32 s65, s17, 10
	v_or_b32_e32 v2, s65, v3
	s_mov_b32 s22, 0x51eb851f
	v_mul_hi_i32 v4, v2, s22
	v_lshrrev_b32_e32 v5, 31, v4
	v_ashrrev_i32_e32 v4, 7, v4
	v_add_u32_e32 v4, v4, v5
	v_mul_i32_i24_e32 v5, 0x190, v4
	v_sub_u32_e32 v2, v2, v5
	s_movk_i32 s21, 0x180
	s_add_i32 s18, s16, 8
	v_cmp_gt_i32_e32 vcc, s21, v2
	s_min_i32 s17, s18, 24
	s_lshl_b32 s66, s17, 10
	v_cndmask_b32_e32 v2, 0, v2, vcc
	v_mad_i32_i24 v2, v4, s21, v2
	v_or_b32_e32 v4, s66, v3
	v_mul_hi_i32 v5, v4, s22
	v_lshrrev_b32_e32 v6, 31, v5
	v_ashrrev_i32_e32 v5, 7, v5
	v_add_u32_e32 v5, v5, v6
	v_mul_i32_i24_e32 v6, 0x190, v5
	v_sub_u32_e32 v4, v4, v6
	s_add_i32 s19, s16, 16
	v_cmp_gt_i32_e32 vcc, s21, v4
	s_min_i32 s17, s19, 24
	s_lshl_b32 s67, s17, 10
	v_cndmask_b32_e32 v4, 0, v4, vcc
	v_mad_i32_i24 v4, v5, s21, v4
	v_or_b32_e32 v5, s67, v3
	v_mul_hi_i32 v6, v5, s22
	v_lshrrev_b32_e32 v7, 31, v6
	v_ashrrev_i32_e32 v6, 7, v6
	v_add_u32_e32 v6, v6, v7
	v_mul_i32_i24_e32 v7, 0x190, v6
	v_sub_u32_e32 v5, v5, v7
	s_min_i32 s17, s16, 0
	v_cmp_gt_i32_e32 vcc, s21, v5
	s_lshl_b32 s68, s17, 10
	s_add_i32 s20, s68, 0x6000
	v_cndmask_b32_e32 v5, 0, v5, vcc
	v_mad_i32_i24 v6, v6, s21, v5
	v_or_b32_e32 v5, s20, v3
	v_mul_hi_i32 v7, v5, s22
	v_lshrrev_b32_e32 v8, 31, v7
	v_ashrrev_i32_e32 v7, 7, v7
	v_add_u32_e32 v7, v7, v8
	v_mul_i32_i24_e32 v8, 0x190, v7
	v_sub_u32_e32 v5, v5, v8
	v_cmp_gt_i32_e32 vcc, s21, v5
	s_min_i32 s16, s16, 17
	s_lshl_b32 s69, s16, 10
	v_cndmask_b32_e32 v5, 0, v5, vcc
	v_mad_i32_i24 v16, v7, s21, v5
	v_or_b32_e32 v5, s69, v3
	s_mov_b32 s21, 0x38e38e39
	v_mul_hi_i32 v7, v5, s21
	v_lshrrev_b32_e32 v8, 31, v7
	v_ashrrev_i32_e32 v7, 5, v7
	v_add_u32_e32 v7, v7, v8
	s_movk_i32 s23, 0x90
	v_mul_lo_u32 v8, v7, s23
	v_sub_u32_e32 v5, v5, v8
	s_movk_i32 s22, 0x80
	v_cmp_gt_i32_e32 vcc, s22, v5
	s_movk_i32 s34, 0x1200
	v_ashrrev_i32_e32 v179, 8, v176
	v_cndmask_b32_e32 v8, 0, v5, vcc
	v_mad_u64_u32 v[18:19], s[16:17], v7, s34, v[8:9]
	s_min_i32 s16, s18, 17
	s_lshl_b32 s70, s16, 10
	v_or_b32_e32 v5, s70, v3
	v_mul_hi_i32 v7, v5, s21
	v_lshrrev_b32_e32 v8, 31, v7
	v_ashrrev_i32_e32 v7, 5, v7
	v_add_u32_e32 v7, v7, v8
	v_mul_lo_u32 v8, v7, s23
	v_sub_u32_e32 v5, v5, v8
	v_cmp_gt_i32_e32 vcc, s22, v5
	s_add_i32 s18, s65, 0
	s_mov_b32 m0, s18
	v_cndmask_b32_e32 v8, 0, v5, vcc
	v_mad_u64_u32 v[20:21], s[16:17], v7, s34, v[8:9]
	s_min_i32 s16, s19, 17
	s_lshl_b32 s71, s16, 10
	v_or_b32_e32 v3, s71, v3
	v_mul_hi_i32 v5, v3, s21
	v_lshrrev_b32_e32 v7, 31, v5
	v_ashrrev_i32_e32 v5, 5, v5
	v_add_u32_e32 v5, v5, v7
	v_mul_lo_u32 v7, v5, s23
	s_add_i32 s19, s66, 0
	v_sub_u32_e32 v3, v3, v7
	global_load_lds_dwordx4 v2, s[0:1]
	s_mov_b32 m0, s19
	s_add_i32 s21, s67, 0
	v_cmp_gt_i32_e32 vcc, s22, v3
	global_load_lds_dwordx4 v4, s[0:1]
	s_mov_b32 m0, s21
	s_add_i32 s22, s68, 0
	global_load_lds_dwordx4 v6, s[0:1]
	s_add_i32 m0, s22, 0x6000
	v_readlane_b32 s23, v255, 50
	global_load_lds_dwordx4 v16, s[0:1]
	s_add_i32 m0, s23, s69
	v_cndmask_b32_e32 v8, 0, v3, vcc
	global_load_lds_dwordx4 v18, s[24:25]
	s_add_i32 m0, s23, s70
	v_mad_u64_u32 v[22:23], s[16:17], v5, s34, v[8:9]
	global_load_lds_dwordx4 v20, s[24:25]
	s_add_i32 m0, s23, s71
	s_add_u32 s16, s0, 0x6000
	global_load_lds_dwordx4 v22, s[24:25]
	s_addc_u32 s17, s1, 0
	s_add_i32 m0, s18, 0x6400
	v_mov_b32_e32 v19, v207
	global_load_lds_dwordx4 v2, s[16:17]
	s_add_i32 m0, s19, 0x6400
	v_lshl_add_u64 v[8:9], s[24:25], 0, v[18:19]
	global_load_lds_dwordx4 v4, s[16:17]
	s_add_i32 m0, s21, 0x6400
	v_mov_b32_e32 v21, v207
	global_load_lds_dwordx4 v6, s[16:17]
	s_add_i32 m0, s22, 0xc400
	v_lshl_add_u64 v[10:11], s[24:25], 0, v[20:21]
	global_load_lds_dwordx4 v16, s[16:17]
	v_readlane_b32 s16, v255, 51
	v_lshl_add_u64 v[8:9], v[8:9], 0, s[8:9]
	s_add_i32 m0, s16, s69
	v_mov_b32_e32 v23, v207
	global_load_lds_dwordx4 v[8:9], off
	v_lshl_add_u64 v[8:9], v[10:11], 0, s[8:9]
	s_add_i32 m0, s16, s70
	v_lshl_add_u64 v[12:13], s[24:25], 0, v[22:23]
	global_load_lds_dwordx4 v[8:9], off
	s_add_i32 m0, s16, s71
	v_lshl_add_u64 v[8:9], v[12:13], 0, s[8:9]
	s_add_u32 s0, s0, 0xc000
	global_load_lds_dwordx4 v[8:9], off
	s_addc_u32 s1, s1, 0
	s_add_i32 m0, s18, 0xc800
	s_add_i32 s16, s20, 0
	global_load_lds_dwordx4 v2, s[0:1]
	s_add_i32 m0, s19, 0xc800
	v_lshl_or_b32 v3, v179, 5, v24
	global_load_lds_dwordx4 v4, s[0:1]
	s_add_i32 m0, s21, 0xc800
	s_mov_b32 s36, 0
	global_load_lds_dwordx4 v6, s[0:1]
	s_add_i32 m0, s16, 0xc800
	v_mov_b32_e32 v5, v207
	global_load_lds_dwordx4 v16, s[0:1]
	s_movk_i32 s0, 0x190
	v_mul_lo_u32 v184, v3, s0
	s_waitcnt vmcnt(0)
	s_barrier
; #define LAS __attribute__((address_space(3)))
; __device__ __forceinline__ void attn_unit(const bf16_t* Qrows  , const bf16_t* Kbh, const bf16_t* Vbh, int nkeys, bf16_t* Orows, LAS unsigned char* lds) {
;     ...
;     f32x16 sA, sB;
;     { const LAS unsigned char* kp = lds + (kh * 32 + l32) * KPITCH + hi * 16;
; #pragma unroll
;       for (int r = 0; r < 16; ++r) sA[r] = 0.f;
; #pragma unroll
;       for (int i = 0; i < 12; ++i) { const bf16x8 kf = *(const LAS bf16x8*)(kp + i * 32); sA = __builtin_amdgcn_mfma_f32_32x32x16_bf16(kf, qf[i], sA, 0, 0, 0); } }
;     int k1 = 1, v0 = 0;
;     int j = 0;
	v_add3_u32 v185, 0, v184, v206
	ds_read_b128 v[8:11], v185
	ds_read_b128 v[12:15], v185 offset:32
	s_waitcnt vmcnt(0) lgkmcnt(0)
	v_mfma_f32_32x32x16_bf16 v[66:81], v[8:11], v[142:145], 0
	s_add_u32 s0, s84, s15
	v_mov_b32_e32 v3, v207
	v_mov_b32_e32 v7, v207
	v_mov_b32_e32 v17, v207
	s_mov_b32 s50, s36
	s_mov_b32 s51, s36
	s_addc_u32 s1, s85, s13
	v_mfma_f32_32x32x16_bf16 v[66:81], v[12:15], v[138:141], v[66:81]
	ds_read_b128 v[8:11], v185 offset:64
	ds_read_b128 v[12:15], v185 offset:96
	s_mov_b32 s37, s36
	s_mov_b32 s38, s36
	s_mov_b32 s39, s36
	s_mov_b32 s40, s36
	s_mov_b32 s41, s36
	s_mov_b32 s42, s36
	s_waitcnt lgkmcnt(1)
	v_mfma_f32_32x32x16_bf16 v[66:81], v[8:11], v[134:137], v[66:81]
	s_mov_b32 s43, s36
	s_mov_b32 s44, s36
	s_mov_b32 s45, s36
	s_mov_b32 s46, s36
	s_mov_b32 s47, s36
	s_mov_b32 s48, s36
	s_mov_b32 s49, s36
	s_waitcnt lgkmcnt(0)
	v_mfma_f32_32x32x16_bf16 v[66:81], v[12:15], v[130:133], v[66:81]
	ds_read_b128 v[8:11], v185 offset:128
	ds_read_b128 v[12:15], v185 offset:160
	v_mov_b64_e32 v[64:65], s[50:51]
	v_lshlrev_b32_e32 v181, 6, v179
	v_lshl_add_u64 v[150:151], s[0:1], 0, v[2:3]
	v_lshl_add_u64 v[152:153], s[0:1], 0, v[4:5]
	v_lshl_add_u64 v[154:155], s[0:1], 0, v[6:7]
	v_lshl_add_u64 v[156:157], s[0:1], 0, v[16:17]
	s_mov_b64 s[80:81], s[0:1]
	v_mov_b32_e32 v208, v2
	v_mov_b32_e32 v209, v4
	v_mov_b32_e32 v210, v6
	v_mov_b32_e32 v211, v16
	s_waitcnt lgkmcnt(1)
	v_mfma_f32_32x32x16_bf16 v[66:81], v[8:11], v[126:129], v[66:81]
	s_add_u32 s0, s84, s14
	v_mov_b64_e32 v[50:51], s[36:37]
	v_mul_u32_u24_e32 v182, 0x90, v24
	s_addc_u32 s1, s85, s12
	v_mov_b64_e32 v[62:63], s[48:49]
	v_mov_b64_e32 v[60:61], s[46:47]
	v_mov_b64_e32 v[58:59], s[44:45]
	s_waitcnt lgkmcnt(0)
	v_mfma_f32_32x32x16_bf16 v[66:81], v[12:15], v[122:125], v[66:81]
	ds_read_b128 v[8:11], v185 offset:192
	ds_read_b128 v[12:15], v185 offset:224
	v_mov_b64_e32 v[56:57], s[42:43]
	v_mov_b64_e32 v[54:55], s[40:41]
	v_mov_b64_e32 v[52:53], s[38:39]
	v_lshl_add_u64 v[158:159], s[0:1], 0, v[18:19]
	v_lshl_add_u64 v[160:161], s[0:1], 0, v[20:21]
	v_lshl_add_u64 v[162:163], s[0:1], 0, v[22:23]
	s_mov_b64 s[82:83], s[0:1]
	v_mov_b32_e32 v212, v18
	v_mov_b32_e32 v213, v20
	v_mov_b32_e32 v214, v22
	s_waitcnt lgkmcnt(1)
	v_mfma_f32_32x32x16_bf16 v[66:81], v[8:11], v[118:121], v[66:81]
	ds_read_b128 v[8:11], v185 offset:256
	v_mov_b64_e32 v[34:35], v[50:51]
	v_mov_b64_e32 v[18:19], v[50:51]
	s_mov_b32 s14, 1
	v_mov_b32_e32 v186, 0
	v_mov_b32_e32 v183, 0xf149f2ca
	v_mov_b64_e32 v[36:37], v[52:53]
	s_waitcnt lgkmcnt(1)
	v_mfma_f32_32x32x16_bf16 v[66:81], v[12:15], v[114:117], v[66:81]
	ds_read_b128 v[12:15], v185 offset:288
	v_mov_b64_e32 v[38:39], v[54:55]
	v_mov_b64_e32 v[40:41], v[56:57]
	v_mov_b64_e32 v[42:43], v[58:59]
	v_mov_b64_e32 v[44:45], v[60:61]
	v_mov_b64_e32 v[46:47], v[62:63]
	v_mov_b64_e32 v[48:49], v[64:65]
	s_waitcnt lgkmcnt(1)
	v_mfma_f32_32x32x16_bf16 v[66:81], v[8:11], v[110:113], v[66:81]
	ds_read_b128 v[8:11], v185 offset:320
	v_mov_b64_e32 v[20:21], v[52:53]
	v_mov_b64_e32 v[22:23], v[54:55]
	v_mov_b64_e32 v[24:25], v[56:57]
	v_mov_b64_e32 v[26:27], v[58:59]
	v_mov_b64_e32 v[28:29], v[60:61]
	v_mov_b64_e32 v[30:31], v[62:63]
	s_waitcnt lgkmcnt(1)
	v_mfma_f32_32x32x16_bf16 v[66:81], v[12:15], v[106:109], v[66:81]
	ds_read_b128 v[12:15], v185 offset:352
	v_mov_b64_e32 v[32:33], v[64:65]
	s_waitcnt lgkmcnt(1)
	v_mfma_f32_32x32x16_bf16 v[66:81], v[8:11], v[102:105], v[66:81]
	v_add_u32_e32 v8, s23, v181
	v_add3_u32 v187, v8, v206, v182
	s_waitcnt lgkmcnt(0)
	v_mfma_f32_32x32x16_bf16 v[66:81], v[12:15], v[98:101], v[66:81]
	v_mov_b64_e32 v[2:3], v[50:51]
	v_mov_b64_e32 v[4:5], v[52:53]
	v_mov_b64_e32 v[6:7], v[54:55]
	v_mov_b64_e32 v[8:9], v[56:57]
	v_mov_b64_e32 v[10:11], v[58:59]
	v_mov_b64_e32 v[12:13], v[60:61]
	v_mov_b64_e32 v[14:15], v[62:63]
	v_mov_b64_e32 v[16:17], v[64:65]
	s_nop 7
	s_nop 7
	v_max_f32_e32 v150, v66, v67
	v_max3_f32 v150, v150, v68, v69
	v_max3_f32 v150, v150, v70, v71
	v_max3_f32 v150, v150, v72, v73
	v_max3_f32 v150, v150, v74, v75
	v_max3_f32 v150, v150, v76, v77
	v_max3_f32 v150, v150, v78, v79
	v_max3_f32 v150, v150, v80, v81
	v_mov_b32_e32 v151, v150
	s_nop 1
	v_permlane32_swap_b32_e32 v151, v150
	v_max_f32_e32 v150, v150, v151
	s_branch .LBB0_1236
; #define ATT_DMAK(tile, slot) do { _Pragma("unroll") for (int i = 0; i < 4; ++i) { const int pc = (wv + 8 * i) < 25 ? (wv + 8 * i) : 24; \
;         __builtin_amdgcn_global_load_lds((const unsigned*)((const char*)Kbh + (size_t)(tile) * (64 * 384) + doffK[i]), (LAS unsigned*)(lds + (slot) * KT_BYTES + pc * 1024), 16, 0, 0); } } while (0)
; #define ATT_DMAV(tile, slot) do { _Pragma("unroll") for (int i = 0; i < 3; ++i) { const int pc = (wv + 8 * i) < 18 ? (wv + 8 * i) : 17; \
;         __builtin_amdgcn_global_load_lds((const unsigned*)((const char*)Vbh + (size_t)(tile) * 128 + doffV[i]), (LAS unsigned*)(lds + VRING + (slot) * VT_BYTES + pc * 1024), 16, 0, 0); } } while (0)
; #define ATT_SYNC(full) do { if (full) asm volatile("s_waitcnt vmcnt(7)" ::: "memory"); else asm volatile("s_waitcnt vmcnt(0)" ::: "memory"); \
;         __builtin_amdgcn_s_barrier(); asm volatile("" ::: "memory"); } while (0)
; __device__ __forceinline__ void attn_unit(const bf16_t* Qrows  , const bf16_t* Kbh, const bf16_t* Vbh, int nkeys, bf16_t* Orows, LAS unsigned char* lds) {
;     ...
;         k1 = k1 == 2 ? 0 : k1 + 1; v0 = v0 == 2 ? 0 : v0 + 1;
;         ATT_SYNC(j + 3 < nt);
;         if (j + 4 < nt) ATT_DMAK(j + 4, v0);
;         if (j + 3 < nt) ATT_DMAV(j + 3, v0 == 0 ? 2 : v0 - 1);
;         ATT_STEP(sB, sA, true, k1, v0);
;         k1 = k1 == 2 ? 0 : k1 + 1; v0 = v0 == 2 ? 0 : v0 + 1;
;     }
.LBB0_1235:
	s_add_i32 s15, s14, 1
	s_cmp_lg_u32 s14, 2
	s_cselect_b32 s14, s15, 0
	s_mul_i32 s15, s14, 0x6400
	v_add_u32_e32 v70, s15, v185
	ds_read_b128 v[66:69], v70
	ds_read_b128 v[166:169], v70 offset:32
	ds_read_b128 v[170:173], v70 offset:64
	ds_read_b128 v[188:191], v70 offset:96
	ds_read_b128 v[192:195], v70 offset:128
	ds_read_b128 v[196:199], v70 offset:160
	ds_read_b128 v[200:203], v70 offset:192
	ds_read_b128 v[216:219], v70 offset:224
	ds_read_b128 v[220:223], v70 offset:256
	ds_read_b128 v[224:227], v70 offset:288
	ds_read_b128 v[228:231], v70 offset:320
	ds_read_b128 v[146:149], v70 offset:352
	s_waitcnt lgkmcnt(11)
	v_mfma_f32_32x32x16_bf16 v[66:81], v[66:69], v[142:145], 0
	v_sub_f32_e32 v82, v82, v183
	v_exp_f32_e32 v82, v82
	v_sub_f32_e32 v94, v94, v183
	v_exp_f32_e32 v94, v94
	v_add_f32_e32 v165, 0, v82
	v_add_f32_e32 v165, v94, v165
	s_waitcnt lgkmcnt(10)
	v_mfma_f32_32x32x16_bf16 v[66:81], v[166:169], v[138:141], v[66:81]
	v_sub_f32_e32 v83, v83, v183
	v_exp_f32_e32 v83, v83
	v_sub_f32_e32 v95, v95, v183
	v_exp_f32_e32 v95, v95
	v_add_f32_e32 v165, v83, v165
	v_cvt_pk_bf16_f32 v82, v82, v83
	v_add_f32_e32 v165, v95, v165
	v_sub_f32_e32 v83, v84, v183
	s_waitcnt lgkmcnt(9)
	v_mfma_f32_32x32x16_bf16 v[66:81], v[170:173], v[134:137], v[66:81]
	v_exp_f32_e32 v83, v83
	v_sub_f32_e32 v96, v96, v183
	v_add_f32_e32 v84, v83, v165
	v_exp_f32_e32 v165, v96
	s_nop 0
	v_add_f32_e32 v84, v165, v84
	s_waitcnt lgkmcnt(8)
	v_mfma_f32_32x32x16_bf16 v[66:81], v[188:191], v[130:133], v[66:81]
	v_sub_f32_e32 v85, v85, v183
	v_exp_f32_e32 v85, v85
	v_sub_f32_e32 v96, v97, v183
	v_exp_f32_e32 v97, v96
	v_cvt_pk_bf16_f32 v96, v94, v95
	v_add_f32_e32 v84, v85, v84
	v_cvt_pk_bf16_f32 v83, v83, v85
	v_add_f32_e32 v84, v97, v84
	v_cvt_pk_bf16_f32 v97, v165, v97
	s_waitcnt lgkmcnt(7)
	v_mfma_f32_32x32x16_bf16 v[66:81], v[192:195], v[126:129], v[66:81]
	v_sub_f32_e32 v85, v86, v183
	v_exp_f32_e32 v85, v85
	s_nop 0
	v_add_f32_e32 v84, v85, v84
	s_waitcnt lgkmcnt(6)
	v_mfma_f32_32x32x16_bf16 v[66:81], v[196:199], v[122:125], v[66:81]
	v_sub_f32_e32 v86, v87, v183
	v_exp_f32_e32 v86, v86
	s_nop 0
	v_add_f32_e32 v87, v86, v84
	v_cvt_pk_bf16_f32 v84, v85, v86
	s_waitcnt lgkmcnt(5)
	v_mfma_f32_32x32x16_bf16 v[66:81], v[200:203], v[118:121], v[66:81]
	v_sub_f32_e32 v85, v88, v183
	v_exp_f32_e32 v85, v85
	s_nop 0
	v_add_f32_e32 v86, v85, v87
	s_waitcnt lgkmcnt(4)
	v_mfma_f32_32x32x16_bf16 v[66:81], v[216:219], v[114:117], v[66:81]
	v_sub_f32_e32 v87, v89, v183
	v_exp_f32_e32 v87, v87
	s_nop 0
	v_add_f32_e32 v86, v87, v86
	v_cvt_pk_bf16_f32 v85, v85, v87
	v_sub_f32_e32 v87, v90, v183
	v_exp_f32_e32 v90, v87
	s_waitcnt lgkmcnt(3)
	v_mfma_f32_32x32x16_bf16 v[66:81], v[220:223], v[110:113], v[66:81]
	v_add_u32_e32 v165, s13, v187
	v_add_f32_e32 v94, v90, v86
	ds_read_b128 v[86:89], v165
	ds_read_b128 v[166:169], v165 offset:32
	s_waitcnt lgkmcnt(4)
	v_mfma_f32_32x32x16_bf16 v[66:81], v[224:227], v[106:109], v[66:81]
	v_sub_f32_e32 v91, v91, v183
	ds_read_b128 v[170:173], v165 offset:4608
	ds_read_b128 v[188:191], v165 offset:4640
	v_exp_f32_e32 v91, v91
	s_nop 0
	v_add_f32_e32 v95, v91, v94
	v_cvt_pk_bf16_f32 v94, v90, v91
	s_waitcnt lgkmcnt(5)
	v_mfma_f32_32x32x16_bf16 v[66:81], v[228:231], v[102:105], v[66:81]
	v_sub_f32_e32 v90, v92, v183
	ds_read_b128 v[192:195], v165 offset:9216
	ds_read_b128 v[196:199], v165 offset:9248
	v_exp_f32_e32 v90, v90
	s_nop 0
	v_add_f32_e32 v91, v90, v95
	v_sub_f32_e32 v92, v93, v183
	v_exp_f32_e32 v92, v92
	s_waitcnt lgkmcnt(6)
	v_mfma_f32_32x32x16_bf16 v[66:81], v[146:149], v[98:101], v[66:81]
	v_add_f32_e32 v186, v92, v91
	v_cvt_pk_bf16_f32 v95, v90, v92
	ds_read_b128 v[90:93], v165 offset:13824
	ds_read_b128 v[146:149], v165 offset:13856
	s_waitcnt lgkmcnt(0)
	v_mfma_f32_32x32x16_bf16 v[50:65], v[86:89], v[82:85], v[50:65]
	v_add_f32_e32 v186, v164, v186
	v_mfma_f32_32x32x16_bf16 v[34:49], v[170:173], v[82:85], v[34:49]
	v_mfma_f32_32x32x16_bf16 v[18:33], v[192:195], v[82:85], v[18:33]
	v_max_f32_e32 v150, v66, v67
	v_max3_f32 v150, v150, v68, v69
	v_mfma_f32_32x32x16_bf16 v[2:17], v[90:93], v[82:85], v[2:17]
	v_max3_f32 v150, v150, v70, v71
	v_max3_f32 v150, v150, v72, v73
	v_mfma_f32_32x32x16_bf16 v[50:65], v[166:169], v[94:97], v[50:65]
	v_max3_f32 v150, v150, v74, v75
	v_max3_f32 v150, v150, v76, v77
	v_mfma_f32_32x32x16_bf16 v[34:49], v[188:191], v[94:97], v[34:49]
	v_max3_f32 v150, v150, v78, v79
	v_max3_f32 v150, v150, v80, v81
	v_mfma_f32_32x32x16_bf16 v[18:33], v[196:199], v[94:97], v[18:33]
	v_mfma_f32_32x32x16_bf16 v[2:17], v[146:149], v[94:97], v[2:17]
	v_mov_b32_e32 v151, v150
	s_nop 1
	v_permlane32_swap_b32_e32 v151, v150
	v_max_f32_e32 v150, v150, v151
	s_add_i32 s13, s14, 1
	s_cmp_lg_u32 s14, 2
	s_cselect_b32 s14, s13, 0
	s_add_i32 s13, s12, 1
	s_cmp_lg_u32 s12, 2
	s_cselect_b32 s36, s13, 0
	s_add_u32 s80, s80, s6
	s_addc_u32 s81, s81, s7
	s_add_u32 s82, s82, s10
	s_addc_u32 s83, s83, s11
	s_add_i32 s63, s63, 2
	s_andn2_b64 vcc, exec, s[0:1]
	s_cbranch_vccz .LBB0_1250

; #define ATT_DMAK(tile, slot) do { _Pragma("unroll") for (int i = 0; i < 4; ++i) { const int pc = (wv + 8 * i) < 25 ? (wv + 8 * i) : 24; \
;         __builtin_amdgcn_global_load_lds((const unsigned*)((const char*)Kbh + (size_t)(tile) * (64 * 384) + doffK[i]), (LAS unsigned*)(lds + (slot) * KT_BYTES + pc * 1024), 16, 0, 0); } } while (0)
; #define ATT_DMAV(tile, slot) do { _Pragma("unroll") for (int i = 0; i < 3; ++i) { const int pc = (wv + 8 * i) < 18 ? (wv + 8 * i) : 17; \
;         __builtin_amdgcn_global_load_lds((const unsigned*)((const char*)Vbh + (size_t)(tile) * 128 + doffV[i]), (LAS unsigned*)(lds + VRING + (slot) * VT_BYTES + pc * 1024), 16, 0, 0); } } while (0)
; #define ATT_SYNC(full) do { if (full) asm volatile("s_waitcnt vmcnt(7)" ::: "memory"); else asm volatile("s_waitcnt vmcnt(0)" ::: "memory"); \
;         __builtin_amdgcn_s_barrier(); asm volatile("" ::: "memory"); } while (0)
; __device__ __forceinline__ void attn_unit(const bf16_t* Qrows  , const bf16_t* Kbh, const bf16_t* Vbh, int nkeys, bf16_t* Orows, LAS unsigned char* lds) {
;     ...
;         ATT_SYNC(true);
;         if (j + 3 < nt) ATT_DMAK(j + 3, v0);
;         ATT_DMAV(j + 2, v0 == 0 ? 2 : v0 - 1);
;         ATT_STEP(sA, sB, true, k1, v0);
.LBB0_1238:
	s_mul_i32 s12, s36, 0x4800
	s_add_i32 s13, s12, 0xffffb800
	s_cmp_lg_u32 s36, 0
	s_cselect_b32 s13, s13, 0x9000
	s_add_i32 s13, s13, 0
	s_add_i32 s13, s13, 0x12c00
	s_add_u32 s16, s82, s2
	s_addc_u32 s17, s83, s3
	s_add_u32 s16, s16, s28
	s_addc_u32 s17, s17, s29
	s_add_i32 m0, s13, s69
	s_nop 0
	global_load_lds_dwordx4 v212, s[16:17]
	s_add_i32 m0, s13, s70
	s_nop 0
	global_load_lds_dwordx4 v213, s[16:17]
	s_add_i32 m0, s13, s71
	s_nop 0
	global_load_lds_dwordx4 v214, s[16:17]
	v_mov_b32_e32 v82, v150
	v_add_f32_e32 v83, 0x41000000, v183
	v_cmp_gt_f32_e32 vcc, v82, v83
	s_cbranch_vccz .LBB0_1240
	v_max_f32_e32 v82, v82, v82
	v_max_f32_e32 v83, v183, v183
	v_max_f32_e32 v83, v83, v82
	v_sub_f32_e32 v82, v183, v83
	v_exp_f32_e32 v82, v82
	v_mov_b32_e32 v183, v83
	v_pk_mul_f32 v[64:65], v[64:65], v[82:83] op_sel_hi:[1,0]
	v_pk_mul_f32 v[62:63], v[62:63], v[82:83] op_sel_hi:[1,0]
	v_pk_mul_f32 v[60:61], v[60:61], v[82:83] op_sel_hi:[1,0]
	v_pk_mul_f32 v[58:59], v[58:59], v[82:83] op_sel_hi:[1,0]
	v_pk_mul_f32 v[56:57], v[56:57], v[82:83] op_sel_hi:[1,0]
	v_pk_mul_f32 v[54:55], v[54:55], v[82:83] op_sel_hi:[1,0]
	v_pk_mul_f32 v[52:53], v[52:53], v[82:83] op_sel_hi:[1,0]
	v_pk_mul_f32 v[50:51], v[50:51], v[82:83] op_sel_hi:[1,0]
	v_pk_mul_f32 v[48:49], v[48:49], v[82:83] op_sel_hi:[1,0]
	v_pk_mul_f32 v[46:47], v[46:47], v[82:83] op_sel_hi:[1,0]
	v_pk_mul_f32 v[44:45], v[44:45], v[82:83] op_sel_hi:[1,0]
	v_pk_mul_f32 v[42:43], v[42:43], v[82:83] op_sel_hi:[1,0]
	v_pk_mul_f32 v[40:41], v[40:41], v[82:83] op_sel_hi:[1,0]
	v_pk_mul_f32 v[38:39], v[38:39], v[82:83] op_sel_hi:[1,0]
	v_pk_mul_f32 v[36:37], v[36:37], v[82:83] op_sel_hi:[1,0]
	v_pk_mul_f32 v[34:35], v[34:35], v[82:83] op_sel_hi:[1,0]
	v_pk_mul_f32 v[32:33], v[32:33], v[82:83] op_sel_hi:[1,0]
	v_pk_mul_f32 v[30:31], v[30:31], v[82:83] op_sel_hi:[1,0]
	v_pk_mul_f32 v[28:29], v[28:29], v[82:83] op_sel_hi:[1,0]
	v_pk_mul_f32 v[26:27], v[26:27], v[82:83] op_sel_hi:[1,0]
	v_pk_mul_f32 v[24:25], v[24:25], v[82:83] op_sel_hi:[1,0]
	v_pk_mul_f32 v[22:23], v[22:23], v[82:83] op_sel_hi:[1,0]
	v_pk_mul_f32 v[20:21], v[20:21], v[82:83] op_sel_hi:[1,0]
	v_pk_mul_f32 v[18:19], v[18:19], v[82:83] op_sel_hi:[1,0]
	v_pk_mul_f32 v[16:17], v[16:17], v[82:83] op_sel_hi:[1,0]
	v_pk_mul_f32 v[14:15], v[14:15], v[82:83] op_sel_hi:[1,0]
	v_pk_mul_f32 v[12:13], v[12:13], v[82:83] op_sel_hi:[1,0]
	v_pk_mul_f32 v[10:11], v[10:11], v[82:83] op_sel_hi:[1,0]
	v_pk_mul_f32 v[8:9], v[8:9], v[82:83] op_sel_hi:[1,0]
	v_pk_mul_f32 v[6:7], v[6:7], v[82:83] op_sel_hi:[1,0]
	v_pk_mul_f32 v[4:5], v[4:5], v[82:83] op_sel_hi:[1,0]
	v_pk_mul_f32 v[2:3], v[2:3], v[82:83] op_sel_hi:[1,0]
	v_mul_f32_e32 v186, v186, v82
.LBB0_1240:
	s_mul_i32 s13, s14, 0x6400
	v_add_u32_e32 v86, s13, v185
	ds_read_b128 v[82:85], v86
	ds_read_b128 v[188:191], v86 offset:32
	ds_read_b128 v[192:195], v86 offset:64
	ds_read_b128 v[196:199], v86 offset:96
	ds_read_b128 v[200:203], v86 offset:128
	ds_read_b128 v[216:219], v86 offset:160
	ds_read_b128 v[220:223], v86 offset:192
	ds_read_b128 v[224:227], v86 offset:224
	ds_read_b128 v[228:231], v86 offset:256
	ds_read_b128 v[232:235], v86 offset:288
	ds_read_b128 v[236:239], v86 offset:320
	ds_read_b128 v[240:243], v86 offset:352
	s_waitcnt lgkmcnt(11)
	v_mfma_f32_32x32x16_bf16 v[82:97], v[82:85], v[142:145], 0
	v_sub_f32_e32 v66, v66, v183
	v_sub_f32_e32 v78, v78, v183
	v_exp_f32_e32 v66, v66
	v_exp_f32_e32 v78, v78
	s_waitcnt lgkmcnt(10)
	v_mfma_f32_32x32x16_bf16 v[82:97], v[188:191], v[138:141], v[82:97]
	v_sub_f32_e32 v67, v67, v183
	v_sub_f32_e32 v79, v79, v183
	v_exp_f32_e32 v67, v67
	v_exp_f32_e32 v79, v79
	v_cvt_pk_bf16_f32 v188, v66, v67
	s_waitcnt lgkmcnt(9)
	v_mfma_f32_32x32x16_bf16 v[82:97], v[192:195], v[134:137], v[82:97]
	v_sub_f32_e32 v68, v68, v183
	v_sub_f32_e32 v80, v80, v183
	v_exp_f32_e32 v68, v68
	v_exp_f32_e32 v80, v80
	s_waitcnt lgkmcnt(8)
	v_mfma_f32_32x32x16_bf16 v[82:97], v[196:199], v[130:133], v[82:97]
	v_sub_f32_e32 v69, v69, v183
	v_sub_f32_e32 v81, v81, v183
	v_exp_f32_e32 v69, v69
	v_exp_f32_e32 v81, v81
	v_cvt_pk_bf16_f32 v194, v78, v79
	v_cvt_pk_bf16_f32 v189, v68, v69
	v_cvt_pk_bf16_f32 v195, v80, v81
	s_waitcnt lgkmcnt(7)
	v_mfma_f32_32x32x16_bf16 v[82:97], v[200:203], v[126:129], v[82:97]
	v_sub_f32_e32 v70, v70, v183
	v_exp_f32_e32 v70, v70
	s_waitcnt lgkmcnt(6)
	v_mfma_f32_32x32x16_bf16 v[82:97], v[216:219], v[122:125], v[82:97]
	v_sub_f32_e32 v71, v71, v183
	v_exp_f32_e32 v71, v71
	s_nop 0
	v_cvt_pk_bf16_f32 v190, v70, v71
	s_waitcnt lgkmcnt(5)
	v_mfma_f32_32x32x16_bf16 v[82:97], v[220:223], v[118:121], v[82:97]
	v_sub_f32_e32 v72, v72, v183
	v_exp_f32_e32 v72, v72
	s_waitcnt lgkmcnt(4)
	v_mfma_f32_32x32x16_bf16 v[82:97], v[224:227], v[114:117], v[82:97]
	v_sub_f32_e32 v73, v73, v183
	v_exp_f32_e32 v73, v73
	s_nop 0
	v_cvt_pk_bf16_f32 v191, v72, v73
	s_waitcnt lgkmcnt(3)
	v_mfma_f32_32x32x16_bf16 v[82:97], v[228:231], v[110:113], v[82:97]
	v_add_u32_e32 v204, s12, v187
	v_sub_f32_e32 v74, v74, v183
	ds_read_b128 v[196:199], v204
	ds_read_b128 v[200:203], v204 offset:32
	v_exp_f32_e32 v74, v74
	s_waitcnt lgkmcnt(4)
	v_mfma_f32_32x32x16_bf16 v[82:97], v[232:235], v[106:109], v[82:97]
	v_sub_f32_e32 v75, v75, v183
	ds_read_b128 v[216:219], v204 offset:4608
	ds_read_b128 v[220:223], v204 offset:4640
	v_exp_f32_e32 v75, v75
	s_nop 0
	v_cvt_pk_bf16_f32 v192, v74, v75
	s_waitcnt lgkmcnt(5)
	v_mfma_f32_32x32x16_bf16 v[82:97], v[236:239], v[102:105], v[82:97]
	v_sub_f32_e32 v76, v76, v183
	ds_read_b128 v[224:227], v204 offset:9216
	ds_read_b128 v[228:231], v204 offset:9248
	v_exp_f32_e32 v76, v76
	s_waitcnt lgkmcnt(6)
	v_mfma_f32_32x32x16_bf16 v[82:97], v[240:243], v[98:101], v[82:97]
	v_sub_f32_e32 v77, v77, v183
	ds_read_b128 v[232:235], v204 offset:13824
	ds_read_b128 v[236:239], v204 offset:13856
	v_exp_f32_e32 v77, v77
	s_nop 0
	v_cvt_pk_bf16_f32 v193, v76, v77
	s_waitcnt lgkmcnt(0)
	v_mfma_f32_32x32x16_bf16 v[50:65], v[196:199], v[188:191], v[50:65]
	v_mfma_f32_32x32x16_bf16 v[34:49], v[216:219], v[188:191], v[34:49]
	v_mfma_f32_32x32x16_bf16 v[18:33], v[224:227], v[188:191], v[18:33]
	v_max_f32_e32 v152, v82, v83
	v_max3_f32 v152, v152, v84, v85
	v_mfma_f32_32x32x16_bf16 v[2:17], v[232:235], v[188:191], v[2:17]
	v_max3_f32 v152, v152, v86, v87
	v_max3_f32 v152, v152, v88, v89
	v_mfma_f32_32x32x16_bf16 v[50:65], v[200:203], v[192:195], v[50:65]
	v_max3_f32 v152, v152, v90, v91
	v_max3_f32 v152, v152, v92, v93
	v_mfma_f32_32x32x16_bf16 v[34:49], v[220:223], v[192:195], v[34:49]
	v_max3_f32 v152, v152, v94, v95
	v_max3_f32 v152, v152, v96, v97
	v_mfma_f32_32x32x16_bf16 v[18:33], v[228:231], v[192:195], v[18:33]
	v_mfma_f32_32x32x16_bf16 v[2:17], v[236:239], v[192:195], v[2:17]
	v_mov_b32_e32 v153, v152
	s_nop 1
	v_permlane32_swap_b32_e32 v153, v152
	v_max_f32_e32 v152, v152, v153
	s_mov_b64 s[12:13], -1
	s_and_b64 vcc, exec, s[0:1]
	s_cbranch_vccz .LBB0_1242
	s_waitcnt vmcnt(0)
	s_mov_b64 s[12:13], 0

.LBB0_1248:
	v_add_f32_e32 v66, 0, v66
	v_add_f32_e32 v66, v78, v66
	v_add_f32_e32 v66, v67, v66
	v_add_f32_e32 v66, v79, v66
	v_add_f32_e32 v66, v68, v66
	v_add_f32_e32 v66, v80, v66
	v_add_f32_e32 v66, v69, v66
	v_add_f32_e32 v66, v81, v66
	v_add_f32_e32 v66, v70, v66
	v_add_f32_e32 v66, v71, v66
	v_add_f32_e32 v66, v72, v66
	v_add_f32_e32 v66, v73, v66
	v_add_f32_e32 v66, v74, v66
	v_add_f32_e32 v66, v75, v66
	v_add_f32_e32 v66, v76, v66
	v_add_f32_e32 v66, v77, v66
	v_add_f32_e32 v164, v186, v66
	v_mov_b32_e32 v66, v152
	v_add_f32_e32 v67, 0x41000000, v183
	v_cmp_gt_f32_e32 vcc, v66, v67
	s_cbranch_vccz .LBB0_1235
	v_max_f32_e32 v66, v66, v66
	v_max_f32_e32 v67, v183, v183
	v_max_f32_e32 v67, v67, v66
	v_sub_f32_e32 v66, v183, v67
	v_exp_f32_e32 v66, v66
	v_mov_b32_e32 v183, v67
	v_pk_mul_f32 v[64:65], v[64:65], v[66:67] op_sel_hi:[1,0]
	v_pk_mul_f32 v[62:63], v[62:63], v[66:67] op_sel_hi:[1,0]
	v_pk_mul_f32 v[60:61], v[60:61], v[66:67] op_sel_hi:[1,0]
	v_pk_mul_f32 v[58:59], v[58:59], v[66:67] op_sel_hi:[1,0]
	v_pk_mul_f32 v[56:57], v[56:57], v[66:67] op_sel_hi:[1,0]
	v_pk_mul_f32 v[54:55], v[54:55], v[66:67] op_sel_hi:[1,0]
	v_pk_mul_f32 v[52:53], v[52:53], v[66:67] op_sel_hi:[1,0]
	v_pk_mul_f32 v[50:51], v[50:51], v[66:67] op_sel_hi:[1,0]
	v_pk_mul_f32 v[48:49], v[48:49], v[66:67] op_sel_hi:[1,0]
	v_pk_mul_f32 v[46:47], v[46:47], v[66:67] op_sel_hi:[1,0]
	v_pk_mul_f32 v[44:45], v[44:45], v[66:67] op_sel_hi:[1,0]
	v_pk_mul_f32 v[42:43], v[42:43], v[66:67] op_sel_hi:[1,0]
	v_pk_mul_f32 v[40:41], v[40:41], v[66:67] op_sel_hi:[1,0]
	v_pk_mul_f32 v[38:39], v[38:39], v[66:67] op_sel_hi:[1,0]
	v_pk_mul_f32 v[36:37], v[36:37], v[66:67] op_sel_hi:[1,0]
	v_pk_mul_f32 v[34:35], v[34:35], v[66:67] op_sel_hi:[1,0]
	v_pk_mul_f32 v[32:33], v[32:33], v[66:67] op_sel_hi:[1,0]
	v_pk_mul_f32 v[30:31], v[30:31], v[66:67] op_sel_hi:[1,0]
	v_pk_mul_f32 v[28:29], v[28:29], v[66:67] op_sel_hi:[1,0]
	v_pk_mul_f32 v[26:27], v[26:27], v[66:67] op_sel_hi:[1,0]
	v_pk_mul_f32 v[24:25], v[24:25], v[66:67] op_sel_hi:[1,0]
	v_pk_mul_f32 v[22:23], v[22:23], v[66:67] op_sel_hi:[1,0]
	v_pk_mul_f32 v[20:21], v[20:21], v[66:67] op_sel_hi:[1,0]
	v_pk_mul_f32 v[18:19], v[18:19], v[66:67] op_sel_hi:[1,0]
	v_pk_mul_f32 v[16:17], v[16:17], v[66:67] op_sel_hi:[1,0]
	v_pk_mul_f32 v[14:15], v[14:15], v[66:67] op_sel_hi:[1,0]
	v_pk_mul_f32 v[12:13], v[12:13], v[66:67] op_sel_hi:[1,0]
	v_pk_mul_f32 v[10:11], v[10:11], v[66:67] op_sel_hi:[1,0]
	v_pk_mul_f32 v[8:9], v[8:9], v[66:67] op_sel_hi:[1,0]
	v_pk_mul_f32 v[6:7], v[6:7], v[66:67] op_sel_hi:[1,0]
	v_pk_mul_f32 v[4:5], v[4:5], v[66:67] op_sel_hi:[1,0]
	v_pk_mul_f32 v[2:3], v[2:3], v[66:67] op_sel_hi:[1,0]
	v_mul_f32_e32 v164, v164, v66
	s_branch .LBB0_1235
